# router logits tile: the 128 activation loads of a 32-row tile now run through a 32-deep register ring with counted waits (was one load, full wait, one MFMA at a time) and the weight LDS reads are issu
# baseline (speedup 1.0000x reference)
; #define LAS __attribute__((address_space(3)))
;     __device__ __forceinline__ bf16_t* H() const { return (bf16_t*)(ws + WS_H); }
; __device__ __forceinline__ void phase_norm2_route(const Frame& F, const Params& P, int l, int nrows, long long dctx) {
;     ...
;     for (int t = F.wid; t < ntile; t += 8) {
;         const int rowbase = r0 + t * 32, myrow = min(rowbase + r32, r1 - 1);
;         const bf16_t* ph = F.H() + (size_t)myrow * DM + hi * 8; const bf16_t* pl = LO + (size_t)myrow * DM + hi * 8;
;         const LAS bf16_t* bh = whi + r32 * WROW + hi * 8; const LAS bf16_t* bl = wlo + r32 * WROW + hi * 8;
;         f32x16 acc = f32x16{};
;         bf16x8 ahA[8], alA[8], ahB[8], alB[8];
; #pragma unroll
;         for (int q = 0; q < 8; ++q) { ahA[q] = *(const bf16x8*)(ph + q * 16); alA[q] = *(const bf16x8*)(pl + q * 16); }
; #pragma unroll
;         for (int bt = 0; bt < 8; bt += 2) {
; #pragma unroll
;             for (int q = 0; q < 8; ++q) { ahB[q] = *(const bf16x8*)(ph + ((bt + 1) * 8 + q) * 16); alB[q] = *(const bf16x8*)(pl + ((bt + 1) * 8 + q) * 16); }
; #pragma unroll
;             for (int q = 0; q < 8; ++q) { const int ks = bt * 8 + q;
;                 const bf16x8 wh = *(const LAS bf16x8*)(bh + ks * 16), wl = *(const LAS bf16x8*)(bl + ks * 16);
;                 acc = __builtin_amdgcn_mfma_f32_32x32x16_bf16(ahA[q], wh, acc, 0, 0, 0); acc = __builtin_amdgcn_mfma_f32_32x32x16_bf16(ahA[q], wl, acc, 0, 0, 0); acc = __builtin_amdgcn_mfma_f32_32x32x16_bf16(alA[q], wh, acc, 0, 0, 0); }
;             if (bt + 2 < 8) {
; #pragma unroll
;                 for (int q = 0; q < 8; ++q) { ahA[q] = *(const bf16x8*)(ph + ((bt + 2) * 8 + q) * 16); alA[q] = *(const bf16x8*)(pl + ((bt + 2) * 8 + q) * 16); }
;             }
; #pragma unroll
;             for (int q = 0; q < 8; ++q) { const int ks = (bt + 1) * 8 + q;
;                 const bf16x8 wh = *(const LAS bf16x8*)(bh + ks * 16), wl = *(const LAS bf16x8*)(bl + ks * 16);
;                 acc = __builtin_amdgcn_mfma_f32_32x32x16_bf16(ahB[q], wh, acc, 0, 0, 0); acc = __builtin_amdgcn_mfma_f32_32x32x16_bf16(ahB[q], wl, acc, 0, 0, 0); acc = __builtin_amdgcn_mfma_f32_32x32x16_bf16(alB[q], wh, acc, 0, 0, 0); }
;         }
.LBB0_936:
	v_add_u32_e32 v2, s89, v1
	v_min_i32_e32 v2, s88, v2
	v_ashrrev_i32_e32 v3, 31, v2
	v_lshlrev_b64 v[18:19], 11, v[2:3]
	v_lshl_add_u64 v[20:21], v[24:25], 0, v[18:19]
	v_lshl_add_u64 v[18:19], v[22:23], 0, v[18:19]
	s_mov_b64 s[8:9], -1
	s_mov_b64 s[22:23], -1
	global_load_dwordx4 v[48:51], v[20:21], off
	global_load_dwordx4 v[52:55], v[18:19], off
	global_load_dwordx4 v[56:59], v[20:21], off offset:32
	global_load_dwordx4 v[60:63], v[18:19], off offset:32
	global_load_dwordx4 v[64:67], v[20:21], off offset:64
	global_load_dwordx4 v[68:71], v[18:19], off offset:64
	global_load_dwordx4 v[72:75], v[20:21], off offset:96
	global_load_dwordx4 v[76:79], v[18:19], off offset:96
	global_load_dwordx4 v[80:83], v[20:21], off offset:128
	global_load_dwordx4 v[84:87], v[18:19], off offset:128
	global_load_dwordx4 v[88:91], v[20:21], off offset:160
	global_load_dwordx4 v[92:95], v[18:19], off offset:160
	global_load_dwordx4 v[96:99], v[20:21], off offset:192
	global_load_dwordx4 v[100:103], v[18:19], off offset:192
	global_load_dwordx4 v[104:107], v[20:21], off offset:224
	global_load_dwordx4 v[108:111], v[18:19], off offset:224
	global_load_dwordx4 v[112:115], v[20:21], off offset:256
	global_load_dwordx4 v[116:119], v[18:19], off offset:256
	global_load_dwordx4 v[120:123], v[20:21], off offset:288
	global_load_dwordx4 v[124:127], v[18:19], off offset:288
	global_load_dwordx4 v[128:131], v[20:21], off offset:320
	global_load_dwordx4 v[132:135], v[18:19], off offset:320
	global_load_dwordx4 v[136:139], v[20:21], off offset:352
	global_load_dwordx4 v[140:143], v[18:19], off offset:352
	global_load_dwordx4 v[148:151], v[20:21], off offset:384
	global_load_dwordx4 v[152:155], v[18:19], off offset:384
	global_load_dwordx4 v[156:159], v[20:21], off offset:416
	global_load_dwordx4 v[160:163], v[18:19], off offset:416
	global_load_dwordx4 v[164:167], v[20:21], off offset:448
	global_load_dwordx4 v[168:171], v[18:19], off offset:448
	global_load_dwordx4 v[172:175], v[20:21], off offset:480
	global_load_dwordx4 v[176:179], v[18:19], off offset:480
	ds_read_b128 v[38:41], v29
	ds_read_b128 v[42:45], v31
	ds_read_b128 v[180:183], v29 offset:32
	ds_read_b128 v[184:187], v31 offset:32
	s_waitcnt vmcnt(31) lgkmcnt(2)
	v_mfma_f32_32x32x16_bf16 v[2:17], v[48:51], v[38:41], 0
	v_mfma_f32_32x32x16_bf16 v[2:17], v[48:51], v[42:45], v[2:17]
	global_load_dwordx4 v[48:51], v[20:21], off offset:512
	s_waitcnt vmcnt(31)
	v_mfma_f32_32x32x16_bf16 v[2:17], v[52:55], v[38:41], v[2:17]
	global_load_dwordx4 v[52:55], v[18:19], off offset:512
	ds_read_b128 v[38:41], v29 offset:64
	ds_read_b128 v[42:45], v31 offset:64
	s_waitcnt vmcnt(31) lgkmcnt(2)
	v_mfma_f32_32x32x16_bf16 v[2:17], v[56:59], v[180:183], v[2:17]
	v_mfma_f32_32x32x16_bf16 v[2:17], v[56:59], v[184:187], v[2:17]
	global_load_dwordx4 v[56:59], v[20:21], off offset:544
	s_waitcnt vmcnt(31)
	v_mfma_f32_32x32x16_bf16 v[2:17], v[60:63], v[180:183], v[2:17]
	global_load_dwordx4 v[60:63], v[18:19], off offset:544
	ds_read_b128 v[180:183], v29 offset:96
	ds_read_b128 v[184:187], v31 offset:96
	s_waitcnt vmcnt(31) lgkmcnt(2)
	v_mfma_f32_32x32x16_bf16 v[2:17], v[64:67], v[38:41], v[2:17]
	v_mfma_f32_32x32x16_bf16 v[2:17], v[64:67], v[42:45], v[2:17]
	global_load_dwordx4 v[64:67], v[20:21], off offset:576
	s_waitcnt vmcnt(31)
	v_mfma_f32_32x32x16_bf16 v[2:17], v[68:71], v[38:41], v[2:17]
	global_load_dwordx4 v[68:71], v[18:19], off offset:576
	ds_read_b128 v[38:41], v29 offset:128
	ds_read_b128 v[42:45], v31 offset:128
	s_waitcnt vmcnt(31) lgkmcnt(2)
	v_mfma_f32_32x32x16_bf16 v[2:17], v[72:75], v[180:183], v[2:17]
	v_mfma_f32_32x32x16_bf16 v[2:17], v[72:75], v[184:187], v[2:17]
	global_load_dwordx4 v[72:75], v[20:21], off offset:608
	s_waitcnt vmcnt(31)
	v_mfma_f32_32x32x16_bf16 v[2:17], v[76:79], v[180:183], v[2:17]
	global_load_dwordx4 v[76:79], v[18:19], off offset:608
	ds_read_b128 v[180:183], v29 offset:160
	ds_read_b128 v[184:187], v31 offset:160
	s_waitcnt vmcnt(31) lgkmcnt(2)
	v_mfma_f32_32x32x16_bf16 v[2:17], v[80:83], v[38:41], v[2:17]
	v_mfma_f32_32x32x16_bf16 v[2:17], v[80:83], v[42:45], v[2:17]
	global_load_dwordx4 v[80:83], v[20:21], off offset:640
	s_waitcnt vmcnt(31)
	v_mfma_f32_32x32x16_bf16 v[2:17], v[84:87], v[38:41], v[2:17]
	global_load_dwordx4 v[84:87], v[18:19], off offset:640
	ds_read_b128 v[38:41], v29 offset:192
	ds_read_b128 v[42:45], v31 offset:192
	s_waitcnt vmcnt(31) lgkmcnt(2)
	v_mfma_f32_32x32x16_bf16 v[2:17], v[88:91], v[180:183], v[2:17]
	v_mfma_f32_32x32x16_bf16 v[2:17], v[88:91], v[184:187], v[2:17]
	global_load_dwordx4 v[88:91], v[20:21], off offset:672
	s_waitcnt vmcnt(31)
	v_mfma_f32_32x32x16_bf16 v[2:17], v[92:95], v[180:183], v[2:17]
	global_load_dwordx4 v[92:95], v[18:19], off offset:672
	ds_read_b128 v[180:183], v29 offset:224
	ds_read_b128 v[184:187], v31 offset:224
	s_waitcnt vmcnt(31) lgkmcnt(2)
	v_mfma_f32_32x32x16_bf16 v[2:17], v[96:99], v[38:41], v[2:17]
	v_mfma_f32_32x32x16_bf16 v[2:17], v[96:99], v[42:45], v[2:17]
	global_load_dwordx4 v[96:99], v[20:21], off offset:704
	s_waitcnt vmcnt(31)
	v_mfma_f32_32x32x16_bf16 v[2:17], v[100:103], v[38:41], v[2:17]
	global_load_dwordx4 v[100:103], v[18:19], off offset:704
	ds_read_b128 v[38:41], v29 offset:256
	ds_read_b128 v[42:45], v31 offset:256
	s_waitcnt vmcnt(31) lgkmcnt(2)
	v_mfma_f32_32x32x16_bf16 v[2:17], v[104:107], v[180:183], v[2:17]
	v_mfma_f32_32x32x16_bf16 v[2:17], v[104:107], v[184:187], v[2:17]
	global_load_dwordx4 v[104:107], v[20:21], off offset:736
	s_waitcnt vmcnt(31)
	v_mfma_f32_32x32x16_bf16 v[2:17], v[108:111], v[180:183], v[2:17]
	global_load_dwordx4 v[108:111], v[18:19], off offset:736
	ds_read_b128 v[180:183], v29 offset:288
	ds_read_b128 v[184:187], v31 offset:288
	s_waitcnt vmcnt(31) lgkmcnt(2)
; #define LAS __attribute__((address_space(3)))
; __device__ __forceinline__ void phase_norm2_route(const Frame& F, const Params& P, int l, int nrows, long long dctx) {
;     ...
;         for (int q = 0; q < 8; ++q) { ahA[q] = *(const bf16x8*)(ph + q * 16); alA[q] = *(const bf16x8*)(pl + q * 16); }
; #pragma unroll
;         for (int bt = 0; bt < 8; bt += 2) {
; #pragma unroll
;             for (int q = 0; q < 8; ++q) { ahB[q] = *(const bf16x8*)(ph + ((bt + 1) * 8 + q) * 16); alB[q] = *(const bf16x8*)(pl + ((bt + 1) * 8 + q) * 16); }
; #pragma unroll
;             for (int q = 0; q < 8; ++q) { const int ks = bt * 8 + q;
;                 const bf16x8 wh = *(const LAS bf16x8*)(bh + ks * 16), wl = *(const LAS bf16x8*)(bl + ks * 16);
;                 acc = __builtin_amdgcn_mfma_f32_32x32x16_bf16(ahA[q], wh, acc, 0, 0, 0); acc = __builtin_amdgcn_mfma_f32_32x32x16_bf16(ahA[q], wl, acc, 0, 0, 0); acc = __builtin_amdgcn_mfma_f32_32x32x16_bf16(alA[q], wh, acc, 0, 0, 0); }
;             if (bt + 2 < 8) {
; #pragma unroll
;                 for (int q = 0; q < 8; ++q) { ahA[q] = *(const bf16x8*)(ph + ((bt + 2) * 8 + q) * 16); alA[q] = *(const bf16x8*)(pl + ((bt + 2) * 8 + q) * 16); }
;             }
; #pragma unroll
;             for (int q = 0; q < 8; ++q) { const int ks = (bt + 1) * 8 + q;
;                 const bf16x8 wh = *(const LAS bf16x8*)(bh + ks * 16), wl = *(const LAS bf16x8*)(bl + ks * 16);
;                 acc = __builtin_amdgcn_mfma_f32_32x32x16_bf16(ahB[q], wh, acc, 0, 0, 0); acc = __builtin_amdgcn_mfma_f32_32x32x16_bf16(ahB[q], wl, acc, 0, 0, 0); acc = __builtin_amdgcn_mfma_f32_32x32x16_bf16(alB[q], wh, acc, 0, 0, 0); }
	v_mfma_f32_32x32x16_bf16 v[2:17], v[112:115], v[38:41], v[2:17]
	v_mfma_f32_32x32x16_bf16 v[2:17], v[112:115], v[42:45], v[2:17]
	global_load_dwordx4 v[112:115], v[20:21], off offset:768
	s_waitcnt vmcnt(31)
	v_mfma_f32_32x32x16_bf16 v[2:17], v[116:119], v[38:41], v[2:17]
	global_load_dwordx4 v[116:119], v[18:19], off offset:768
	ds_read_b128 v[38:41], v29 offset:320
	ds_read_b128 v[42:45], v31 offset:320
	s_waitcnt vmcnt(31) lgkmcnt(2)
	v_mfma_f32_32x32x16_bf16 v[2:17], v[120:123], v[180:183], v[2:17]
	v_mfma_f32_32x32x16_bf16 v[2:17], v[120:123], v[184:187], v[2:17]
	global_load_dwordx4 v[120:123], v[20:21], off offset:800
	s_waitcnt vmcnt(31)
	v_mfma_f32_32x32x16_bf16 v[2:17], v[124:127], v[180:183], v[2:17]
	global_load_dwordx4 v[124:127], v[18:19], off offset:800
	ds_read_b128 v[180:183], v29 offset:352
	ds_read_b128 v[184:187], v31 offset:352
	s_waitcnt vmcnt(31) lgkmcnt(2)
	v_mfma_f32_32x32x16_bf16 v[2:17], v[128:131], v[38:41], v[2:17]
	v_mfma_f32_32x32x16_bf16 v[2:17], v[128:131], v[42:45], v[2:17]
	global_load_dwordx4 v[128:131], v[20:21], off offset:832
	s_waitcnt vmcnt(31)
	v_mfma_f32_32x32x16_bf16 v[2:17], v[132:135], v[38:41], v[2:17]
	global_load_dwordx4 v[132:135], v[18:19], off offset:832
	ds_read_b128 v[38:41], v29 offset:384
	ds_read_b128 v[42:45], v31 offset:384
	s_waitcnt vmcnt(31) lgkmcnt(2)
	v_mfma_f32_32x32x16_bf16 v[2:17], v[136:139], v[180:183], v[2:17]
	v_mfma_f32_32x32x16_bf16 v[2:17], v[136:139], v[184:187], v[2:17]
	global_load_dwordx4 v[136:139], v[20:21], off offset:864
	s_waitcnt vmcnt(31)
	v_mfma_f32_32x32x16_bf16 v[2:17], v[140:143], v[180:183], v[2:17]
	global_load_dwordx4 v[140:143], v[18:19], off offset:864
	ds_read_b128 v[180:183], v29 offset:416
	ds_read_b128 v[184:187], v31 offset:416
	s_waitcnt vmcnt(31) lgkmcnt(2)
	v_mfma_f32_32x32x16_bf16 v[2:17], v[148:151], v[38:41], v[2:17]
	v_mfma_f32_32x32x16_bf16 v[2:17], v[148:151], v[42:45], v[2:17]
	global_load_dwordx4 v[148:151], v[20:21], off offset:896
	s_waitcnt vmcnt(31)
	v_mfma_f32_32x32x16_bf16 v[2:17], v[152:155], v[38:41], v[2:17]
	global_load_dwordx4 v[152:155], v[18:19], off offset:896
	ds_read_b128 v[38:41], v29 offset:448
	ds_read_b128 v[42:45], v31 offset:448
	s_waitcnt vmcnt(31) lgkmcnt(2)
	v_mfma_f32_32x32x16_bf16 v[2:17], v[156:159], v[180:183], v[2:17]
	v_mfma_f32_32x32x16_bf16 v[2:17], v[156:159], v[184:187], v[2:17]
	global_load_dwordx4 v[156:159], v[20:21], off offset:928
	s_waitcnt vmcnt(31)
	v_mfma_f32_32x32x16_bf16 v[2:17], v[160:163], v[180:183], v[2:17]
	global_load_dwordx4 v[160:163], v[18:19], off offset:928
	ds_read_b128 v[180:183], v29 offset:480
	ds_read_b128 v[184:187], v31 offset:480
	s_waitcnt vmcnt(31) lgkmcnt(2)
	v_mfma_f32_32x32x16_bf16 v[2:17], v[164:167], v[38:41], v[2:17]
	v_mfma_f32_32x32x16_bf16 v[2:17], v[164:167], v[42:45], v[2:17]
	global_load_dwordx4 v[164:167], v[20:21], off offset:960
	s_waitcnt vmcnt(31)
	v_mfma_f32_32x32x16_bf16 v[2:17], v[168:171], v[38:41], v[2:17]
	global_load_dwordx4 v[168:171], v[18:19], off offset:960
	ds_read_b128 v[38:41], v29 offset:512
	ds_read_b128 v[42:45], v31 offset:512
	s_waitcnt vmcnt(31) lgkmcnt(2)
	v_mfma_f32_32x32x16_bf16 v[2:17], v[172:175], v[180:183], v[2:17]
	v_mfma_f32_32x32x16_bf16 v[2:17], v[172:175], v[184:187], v[2:17]
	global_load_dwordx4 v[172:175], v[20:21], off offset:992
	s_waitcnt vmcnt(31)
	v_mfma_f32_32x32x16_bf16 v[2:17], v[176:179], v[180:183], v[2:17]
	global_load_dwordx4 v[176:179], v[18:19], off offset:992
	ds_read_b128 v[180:183], v29 offset:544
	ds_read_b128 v[184:187], v31 offset:544
	s_waitcnt vmcnt(31) lgkmcnt(2)
	v_mfma_f32_32x32x16_bf16 v[2:17], v[48:51], v[38:41], v[2:17]
	v_mfma_f32_32x32x16_bf16 v[2:17], v[48:51], v[42:45], v[2:17]
	global_load_dwordx4 v[48:51], v[20:21], off offset:1024
	s_waitcnt vmcnt(31)
	v_mfma_f32_32x32x16_bf16 v[2:17], v[52:55], v[38:41], v[2:17]
	global_load_dwordx4 v[52:55], v[18:19], off offset:1024
	ds_read_b128 v[38:41], v29 offset:576
	ds_read_b128 v[42:45], v31 offset:576
	s_waitcnt vmcnt(31) lgkmcnt(2)
	v_mfma_f32_32x32x16_bf16 v[2:17], v[56:59], v[180:183], v[2:17]
	v_mfma_f32_32x32x16_bf16 v[2:17], v[56:59], v[184:187], v[2:17]
	global_load_dwordx4 v[56:59], v[20:21], off offset:1056
	s_waitcnt vmcnt(31)
	v_mfma_f32_32x32x16_bf16 v[2:17], v[60:63], v[180:183], v[2:17]
	global_load_dwordx4 v[60:63], v[18:19], off offset:1056
	ds_read_b128 v[180:183], v29 offset:608
	ds_read_b128 v[184:187], v31 offset:608
	s_waitcnt vmcnt(31) lgkmcnt(2)
	v_mfma_f32_32x32x16_bf16 v[2:17], v[64:67], v[38:41], v[2:17]
	v_mfma_f32_32x32x16_bf16 v[2:17], v[64:67], v[42:45], v[2:17]
	global_load_dwordx4 v[64:67], v[20:21], off offset:1088
	s_waitcnt vmcnt(31)
	v_mfma_f32_32x32x16_bf16 v[2:17], v[68:71], v[38:41], v[2:17]
	global_load_dwordx4 v[68:71], v[18:19], off offset:1088
	ds_read_b128 v[38:41], v29 offset:640
	ds_read_b128 v[42:45], v31 offset:640
	s_waitcnt vmcnt(31) lgkmcnt(2)
	v_mfma_f32_32x32x16_bf16 v[2:17], v[72:75], v[180:183], v[2:17]
	v_mfma_f32_32x32x16_bf16 v[2:17], v[72:75], v[184:187], v[2:17]
	global_load_dwordx4 v[72:75], v[20:21], off offset:1120
	s_waitcnt vmcnt(31)
	v_mfma_f32_32x32x16_bf16 v[2:17], v[76:79], v[180:183], v[2:17]
	global_load_dwordx4 v[76:79], v[18:19], off offset:1120
	ds_read_b128 v[180:183], v29 offset:672
	ds_read_b128 v[184:187], v31 offset:672
	s_waitcnt vmcnt(31) lgkmcnt(2)
	v_mfma_f32_32x32x16_bf16 v[2:17], v[80:83], v[38:41], v[2:17]
	v_mfma_f32_32x32x16_bf16 v[2:17], v[80:83], v[42:45], v[2:17]
	global_load_dwordx4 v[80:83], v[20:21], off offset:1152
	s_waitcnt vmcnt(31)
; #define LAS __attribute__((address_space(3)))
; __device__ __forceinline__ void phase_norm2_route(const Frame& F, const Params& P, int l, int nrows, long long dctx) {
;     ...
;         for (int q = 0; q < 8; ++q) { ahA[q] = *(const bf16x8*)(ph + q * 16); alA[q] = *(const bf16x8*)(pl + q * 16); }
; #pragma unroll
;         for (int bt = 0; bt < 8; bt += 2) {
; #pragma unroll
;             for (int q = 0; q < 8; ++q) { ahB[q] = *(const bf16x8*)(ph + ((bt + 1) * 8 + q) * 16); alB[q] = *(const bf16x8*)(pl + ((bt + 1) * 8 + q) * 16); }
; #pragma unroll
;             for (int q = 0; q < 8; ++q) { const int ks = bt * 8 + q;
;                 const bf16x8 wh = *(const LAS bf16x8*)(bh + ks * 16), wl = *(const LAS bf16x8*)(bl + ks * 16);
;                 acc = __builtin_amdgcn_mfma_f32_32x32x16_bf16(ahA[q], wh, acc, 0, 0, 0); acc = __builtin_amdgcn_mfma_f32_32x32x16_bf16(ahA[q], wl, acc, 0, 0, 0); acc = __builtin_amdgcn_mfma_f32_32x32x16_bf16(alA[q], wh, acc, 0, 0, 0); }
;             if (bt + 2 < 8) {
; #pragma unroll
;                 for (int q = 0; q < 8; ++q) { ahA[q] = *(const bf16x8*)(ph + ((bt + 2) * 8 + q) * 16); alA[q] = *(const bf16x8*)(pl + ((bt + 2) * 8 + q) * 16); }
;             }
; #pragma unroll
;             for (int q = 0; q < 8; ++q) { const int ks = (bt + 1) * 8 + q;
;                 const bf16x8 wh = *(const LAS bf16x8*)(bh + ks * 16), wl = *(const LAS bf16x8*)(bl + ks * 16);
;                 acc = __builtin_amdgcn_mfma_f32_32x32x16_bf16(ahB[q], wh, acc, 0, 0, 0); acc = __builtin_amdgcn_mfma_f32_32x32x16_bf16(ahB[q], wl, acc, 0, 0, 0); acc = __builtin_amdgcn_mfma_f32_32x32x16_bf16(alB[q], wh, acc, 0, 0, 0); }
	v_mfma_f32_32x32x16_bf16 v[2:17], v[84:87], v[38:41], v[2:17]
	global_load_dwordx4 v[84:87], v[18:19], off offset:1152
	ds_read_b128 v[38:41], v29 offset:704
	ds_read_b128 v[42:45], v31 offset:704
	s_waitcnt vmcnt(31) lgkmcnt(2)
	v_mfma_f32_32x32x16_bf16 v[2:17], v[88:91], v[180:183], v[2:17]
	v_mfma_f32_32x32x16_bf16 v[2:17], v[88:91], v[184:187], v[2:17]
	global_load_dwordx4 v[88:91], v[20:21], off offset:1184
	s_waitcnt vmcnt(31)
	v_mfma_f32_32x32x16_bf16 v[2:17], v[92:95], v[180:183], v[2:17]
	global_load_dwordx4 v[92:95], v[18:19], off offset:1184
	ds_read_b128 v[180:183], v29 offset:736
	ds_read_b128 v[184:187], v31 offset:736
	s_waitcnt vmcnt(31) lgkmcnt(2)
	v_mfma_f32_32x32x16_bf16 v[2:17], v[96:99], v[38:41], v[2:17]
	v_mfma_f32_32x32x16_bf16 v[2:17], v[96:99], v[42:45], v[2:17]
	global_load_dwordx4 v[96:99], v[20:21], off offset:1216
	s_waitcnt vmcnt(31)
	v_mfma_f32_32x32x16_bf16 v[2:17], v[100:103], v[38:41], v[2:17]
	global_load_dwordx4 v[100:103], v[18:19], off offset:1216
	ds_read_b128 v[38:41], v29 offset:768
	ds_read_b128 v[42:45], v31 offset:768
	s_waitcnt vmcnt(31) lgkmcnt(2)
	v_mfma_f32_32x32x16_bf16 v[2:17], v[104:107], v[180:183], v[2:17]
	v_mfma_f32_32x32x16_bf16 v[2:17], v[104:107], v[184:187], v[2:17]
	global_load_dwordx4 v[104:107], v[20:21], off offset:1248
	s_waitcnt vmcnt(31)
	v_mfma_f32_32x32x16_bf16 v[2:17], v[108:111], v[180:183], v[2:17]
	global_load_dwordx4 v[108:111], v[18:19], off offset:1248
	ds_read_b128 v[180:183], v29 offset:800
	ds_read_b128 v[184:187], v31 offset:800
	s_waitcnt vmcnt(31) lgkmcnt(2)
	v_mfma_f32_32x32x16_bf16 v[2:17], v[112:115], v[38:41], v[2:17]
	v_mfma_f32_32x32x16_bf16 v[2:17], v[112:115], v[42:45], v[2:17]
	global_load_dwordx4 v[112:115], v[20:21], off offset:1280
	s_waitcnt vmcnt(31)
	v_mfma_f32_32x32x16_bf16 v[2:17], v[116:119], v[38:41], v[2:17]
	global_load_dwordx4 v[116:119], v[18:19], off offset:1280
	ds_read_b128 v[38:41], v29 offset:832
	ds_read_b128 v[42:45], v31 offset:832
	s_waitcnt vmcnt(31) lgkmcnt(2)
	v_mfma_f32_32x32x16_bf16 v[2:17], v[120:123], v[180:183], v[2:17]
	v_mfma_f32_32x32x16_bf16 v[2:17], v[120:123], v[184:187], v[2:17]
	global_load_dwordx4 v[120:123], v[20:21], off offset:1312
	s_waitcnt vmcnt(31)
	v_mfma_f32_32x32x16_bf16 v[2:17], v[124:127], v[180:183], v[2:17]
	global_load_dwordx4 v[124:127], v[18:19], off offset:1312
	ds_read_b128 v[180:183], v29 offset:864
	ds_read_b128 v[184:187], v31 offset:864
	s_waitcnt vmcnt(31) lgkmcnt(2)
	v_mfma_f32_32x32x16_bf16 v[2:17], v[128:131], v[38:41], v[2:17]
	v_mfma_f32_32x32x16_bf16 v[2:17], v[128:131], v[42:45], v[2:17]
	global_load_dwordx4 v[128:131], v[20:21], off offset:1344
	s_waitcnt vmcnt(31)
	v_mfma_f32_32x32x16_bf16 v[2:17], v[132:135], v[38:41], v[2:17]
	global_load_dwordx4 v[132:135], v[18:19], off offset:1344
	ds_read_b128 v[38:41], v29 offset:896
	ds_read_b128 v[42:45], v31 offset:896
	s_waitcnt vmcnt(31) lgkmcnt(2)
	v_mfma_f32_32x32x16_bf16 v[2:17], v[136:139], v[180:183], v[2:17]
	v_mfma_f32_32x32x16_bf16 v[2:17], v[136:139], v[184:187], v[2:17]
	global_load_dwordx4 v[136:139], v[20:21], off offset:1376
	s_waitcnt vmcnt(31)
	v_mfma_f32_32x32x16_bf16 v[2:17], v[140:143], v[180:183], v[2:17]
	global_load_dwordx4 v[140:143], v[18:19], off offset:1376
	ds_read_b128 v[180:183], v29 offset:928
	ds_read_b128 v[184:187], v31 offset:928
	s_waitcnt vmcnt(31) lgkmcnt(2)
	v_mfma_f32_32x32x16_bf16 v[2:17], v[148:151], v[38:41], v[2:17]
	v_mfma_f32_32x32x16_bf16 v[2:17], v[148:151], v[42:45], v[2:17]
	global_load_dwordx4 v[148:151], v[20:21], off offset:1408
	s_waitcnt vmcnt(31)
	v_mfma_f32_32x32x16_bf16 v[2:17], v[152:155], v[38:41], v[2:17]
	global_load_dwordx4 v[152:155], v[18:19], off offset:1408
	ds_read_b128 v[38:41], v29 offset:960
	ds_read_b128 v[42:45], v31 offset:960
	s_waitcnt vmcnt(31) lgkmcnt(2)
	v_mfma_f32_32x32x16_bf16 v[2:17], v[156:159], v[180:183], v[2:17]
	v_mfma_f32_32x32x16_bf16 v[2:17], v[156:159], v[184:187], v[2:17]
	global_load_dwordx4 v[156:159], v[20:21], off offset:1440
	s_waitcnt vmcnt(31)
	v_mfma_f32_32x32x16_bf16 v[2:17], v[160:163], v[180:183], v[2:17]
	global_load_dwordx4 v[160:163], v[18:19], off offset:1440
	ds_read_b128 v[180:183], v29 offset:992
	ds_read_b128 v[184:187], v31 offset:992
	s_waitcnt vmcnt(31) lgkmcnt(2)
	v_mfma_f32_32x32x16_bf16 v[2:17], v[164:167], v[38:41], v[2:17]
	v_mfma_f32_32x32x16_bf16 v[2:17], v[164:167], v[42:45], v[2:17]
	global_load_dwordx4 v[164:167], v[20:21], off offset:1472
	s_waitcnt vmcnt(31)
	v_mfma_f32_32x32x16_bf16 v[2:17], v[168:171], v[38:41], v[2:17]
	global_load_dwordx4 v[168:171], v[18:19], off offset:1472
	ds_read_b128 v[38:41], v29 offset:1024
	ds_read_b128 v[42:45], v31 offset:1024
	s_waitcnt vmcnt(31) lgkmcnt(2)
	v_mfma_f32_32x32x16_bf16 v[2:17], v[172:175], v[180:183], v[2:17]
	v_mfma_f32_32x32x16_bf16 v[2:17], v[172:175], v[184:187], v[2:17]
	global_load_dwordx4 v[172:175], v[20:21], off offset:1504
	s_waitcnt vmcnt(31)
	v_mfma_f32_32x32x16_bf16 v[2:17], v[176:179], v[180:183], v[2:17]
	global_load_dwordx4 v[176:179], v[18:19], off offset:1504
	ds_read_b128 v[180:183], v29 offset:1056
	ds_read_b128 v[184:187], v31 offset:1056
	s_waitcnt vmcnt(31) lgkmcnt(2)
	v_mfma_f32_32x32x16_bf16 v[2:17], v[48:51], v[38:41], v[2:17]
	v_mfma_f32_32x32x16_bf16 v[2:17], v[48:51], v[42:45], v[2:17]
	global_load_dwordx4 v[48:51], v[20:21], off offset:1536
	s_waitcnt vmcnt(31)
	v_mfma_f32_32x32x16_bf16 v[2:17], v[52:55], v[38:41], v[2:17]
	global_load_dwordx4 v[52:55], v[18:19], off offset:1536
	ds_read_b128 v[38:41], v29 offset:1088
	ds_read_b128 v[42:45], v31 offset:1088
	s_waitcnt vmcnt(31) lgkmcnt(2)
; #define LAS __attribute__((address_space(3)))
; __device__ __forceinline__ void phase_norm2_route(const Frame& F, const Params& P, int l, int nrows, long long dctx) {
;     ...
;         for (int q = 0; q < 8; ++q) { ahA[q] = *(const bf16x8*)(ph + q * 16); alA[q] = *(const bf16x8*)(pl + q * 16); }
; #pragma unroll
;         for (int bt = 0; bt < 8; bt += 2) {
; #pragma unroll
;             for (int q = 0; q < 8; ++q) { ahB[q] = *(const bf16x8*)(ph + ((bt + 1) * 8 + q) * 16); alB[q] = *(const bf16x8*)(pl + ((bt + 1) * 8 + q) * 16); }
; #pragma unroll
;             for (int q = 0; q < 8; ++q) { const int ks = bt * 8 + q;
;                 const bf16x8 wh = *(const LAS bf16x8*)(bh + ks * 16), wl = *(const LAS bf16x8*)(bl + ks * 16);
;                 acc = __builtin_amdgcn_mfma_f32_32x32x16_bf16(ahA[q], wh, acc, 0, 0, 0); acc = __builtin_amdgcn_mfma_f32_32x32x16_bf16(ahA[q], wl, acc, 0, 0, 0); acc = __builtin_amdgcn_mfma_f32_32x32x16_bf16(alA[q], wh, acc, 0, 0, 0); }
;             if (bt + 2 < 8) {
; #pragma unroll
;                 for (int q = 0; q < 8; ++q) { ahA[q] = *(const bf16x8*)(ph + ((bt + 2) * 8 + q) * 16); alA[q] = *(const bf16x8*)(pl + ((bt + 2) * 8 + q) * 16); }
;             }
; #pragma unroll
;             for (int q = 0; q < 8; ++q) { const int ks = (bt + 1) * 8 + q;
;                 const bf16x8 wh = *(const LAS bf16x8*)(bh + ks * 16), wl = *(const LAS bf16x8*)(bl + ks * 16);
;                 acc = __builtin_amdgcn_mfma_f32_32x32x16_bf16(ahB[q], wh, acc, 0, 0, 0); acc = __builtin_amdgcn_mfma_f32_32x32x16_bf16(ahB[q], wl, acc, 0, 0, 0); acc = __builtin_amdgcn_mfma_f32_32x32x16_bf16(alB[q], wh, acc, 0, 0, 0); }
	v_mfma_f32_32x32x16_bf16 v[2:17], v[56:59], v[180:183], v[2:17]
	v_mfma_f32_32x32x16_bf16 v[2:17], v[56:59], v[184:187], v[2:17]
	global_load_dwordx4 v[56:59], v[20:21], off offset:1568
	s_waitcnt vmcnt(31)
	v_mfma_f32_32x32x16_bf16 v[2:17], v[60:63], v[180:183], v[2:17]
	global_load_dwordx4 v[60:63], v[18:19], off offset:1568
	ds_read_b128 v[180:183], v29 offset:1120
	ds_read_b128 v[184:187], v31 offset:1120
	s_waitcnt vmcnt(31) lgkmcnt(2)
	v_mfma_f32_32x32x16_bf16 v[2:17], v[64:67], v[38:41], v[2:17]
	v_mfma_f32_32x32x16_bf16 v[2:17], v[64:67], v[42:45], v[2:17]
	global_load_dwordx4 v[64:67], v[20:21], off offset:1600
	s_waitcnt vmcnt(31)
	v_mfma_f32_32x32x16_bf16 v[2:17], v[68:71], v[38:41], v[2:17]
	global_load_dwordx4 v[68:71], v[18:19], off offset:1600
	ds_read_b128 v[38:41], v29 offset:1152
	ds_read_b128 v[42:45], v31 offset:1152
	s_waitcnt vmcnt(31) lgkmcnt(2)
	v_mfma_f32_32x32x16_bf16 v[2:17], v[72:75], v[180:183], v[2:17]
	v_mfma_f32_32x32x16_bf16 v[2:17], v[72:75], v[184:187], v[2:17]
	global_load_dwordx4 v[72:75], v[20:21], off offset:1632
	s_waitcnt vmcnt(31)
	v_mfma_f32_32x32x16_bf16 v[2:17], v[76:79], v[180:183], v[2:17]
	global_load_dwordx4 v[76:79], v[18:19], off offset:1632
	ds_read_b128 v[180:183], v29 offset:1184
	ds_read_b128 v[184:187], v31 offset:1184
	s_waitcnt vmcnt(31) lgkmcnt(2)
	v_mfma_f32_32x32x16_bf16 v[2:17], v[80:83], v[38:41], v[2:17]
	v_mfma_f32_32x32x16_bf16 v[2:17], v[80:83], v[42:45], v[2:17]
	global_load_dwordx4 v[80:83], v[20:21], off offset:1664
	s_waitcnt vmcnt(31)
	v_mfma_f32_32x32x16_bf16 v[2:17], v[84:87], v[38:41], v[2:17]
	global_load_dwordx4 v[84:87], v[18:19], off offset:1664
	ds_read_b128 v[38:41], v29 offset:1216
	ds_read_b128 v[42:45], v31 offset:1216
	s_waitcnt vmcnt(31) lgkmcnt(2)
	v_mfma_f32_32x32x16_bf16 v[2:17], v[88:91], v[180:183], v[2:17]
	v_mfma_f32_32x32x16_bf16 v[2:17], v[88:91], v[184:187], v[2:17]
	global_load_dwordx4 v[88:91], v[20:21], off offset:1696
	s_waitcnt vmcnt(31)
	v_mfma_f32_32x32x16_bf16 v[2:17], v[92:95], v[180:183], v[2:17]
	global_load_dwordx4 v[92:95], v[18:19], off offset:1696
	ds_read_b128 v[180:183], v29 offset:1248
	ds_read_b128 v[184:187], v31 offset:1248
	s_waitcnt vmcnt(31) lgkmcnt(2)
	v_mfma_f32_32x32x16_bf16 v[2:17], v[96:99], v[38:41], v[2:17]
	v_mfma_f32_32x32x16_bf16 v[2:17], v[96:99], v[42:45], v[2:17]
	global_load_dwordx4 v[96:99], v[20:21], off offset:1728
	s_waitcnt vmcnt(31)
	v_mfma_f32_32x32x16_bf16 v[2:17], v[100:103], v[38:41], v[2:17]
	global_load_dwordx4 v[100:103], v[18:19], off offset:1728
	ds_read_b128 v[38:41], v29 offset:1280
	ds_read_b128 v[42:45], v31 offset:1280
	s_waitcnt vmcnt(31) lgkmcnt(2)
	v_mfma_f32_32x32x16_bf16 v[2:17], v[104:107], v[180:183], v[2:17]
	v_mfma_f32_32x32x16_bf16 v[2:17], v[104:107], v[184:187], v[2:17]
	global_load_dwordx4 v[104:107], v[20:21], off offset:1760
	s_waitcnt vmcnt(31)
	v_mfma_f32_32x32x16_bf16 v[2:17], v[108:111], v[180:183], v[2:17]
	global_load_dwordx4 v[108:111], v[18:19], off offset:1760
	ds_read_b128 v[180:183], v29 offset:1312
	ds_read_b128 v[184:187], v31 offset:1312
	s_waitcnt vmcnt(31) lgkmcnt(2)
	v_mfma_f32_32x32x16_bf16 v[2:17], v[112:115], v[38:41], v[2:17]
	v_mfma_f32_32x32x16_bf16 v[2:17], v[112:115], v[42:45], v[2:17]
	global_load_dwordx4 v[112:115], v[20:21], off offset:1792
	s_waitcnt vmcnt(31)
	v_mfma_f32_32x32x16_bf16 v[2:17], v[116:119], v[38:41], v[2:17]
	global_load_dwordx4 v[116:119], v[18:19], off offset:1792
	ds_read_b128 v[38:41], v29 offset:1344
	ds_read_b128 v[42:45], v31 offset:1344
	s_waitcnt vmcnt(31) lgkmcnt(2)
	v_mfma_f32_32x32x16_bf16 v[2:17], v[120:123], v[180:183], v[2:17]
	v_mfma_f32_32x32x16_bf16 v[2:17], v[120:123], v[184:187], v[2:17]
	global_load_dwordx4 v[120:123], v[20:21], off offset:1824
	s_waitcnt vmcnt(31)
	v_mfma_f32_32x32x16_bf16 v[2:17], v[124:127], v[180:183], v[2:17]
	global_load_dwordx4 v[124:127], v[18:19], off offset:1824
	ds_read_b128 v[180:183], v29 offset:1376
	ds_read_b128 v[184:187], v31 offset:1376
	s_waitcnt vmcnt(31) lgkmcnt(2)
	v_mfma_f32_32x32x16_bf16 v[2:17], v[128:131], v[38:41], v[2:17]
	v_mfma_f32_32x32x16_bf16 v[2:17], v[128:131], v[42:45], v[2:17]
	global_load_dwordx4 v[128:131], v[20:21], off offset:1856
	s_waitcnt vmcnt(31)
	v_mfma_f32_32x32x16_bf16 v[2:17], v[132:135], v[38:41], v[2:17]
	global_load_dwordx4 v[132:135], v[18:19], off offset:1856
	ds_read_b128 v[38:41], v29 offset:1408
	ds_read_b128 v[42:45], v31 offset:1408
	s_waitcnt vmcnt(31) lgkmcnt(2)
	v_mfma_f32_32x32x16_bf16 v[2:17], v[136:139], v[180:183], v[2:17]
	v_mfma_f32_32x32x16_bf16 v[2:17], v[136:139], v[184:187], v[2:17]
	global_load_dwordx4 v[136:139], v[20:21], off offset:1888
	s_waitcnt vmcnt(31)
	v_mfma_f32_32x32x16_bf16 v[2:17], v[140:143], v[180:183], v[2:17]
	global_load_dwordx4 v[140:143], v[18:19], off offset:1888
	ds_read_b128 v[180:183], v29 offset:1440
	ds_read_b128 v[184:187], v31 offset:1440
	s_waitcnt vmcnt(31) lgkmcnt(2)
	v_mfma_f32_32x32x16_bf16 v[2:17], v[148:151], v[38:41], v[2:17]
	v_mfma_f32_32x32x16_bf16 v[2:17], v[148:151], v[42:45], v[2:17]
	global_load_dwordx4 v[148:151], v[20:21], off offset:1920
	s_waitcnt vmcnt(31)
	v_mfma_f32_32x32x16_bf16 v[2:17], v[152:155], v[38:41], v[2:17]
	global_load_dwordx4 v[152:155], v[18:19], off offset:1920
	ds_read_b128 v[38:41], v29 offset:1472
	ds_read_b128 v[42:45], v31 offset:1472
	s_waitcnt vmcnt(31) lgkmcnt(2)
	v_mfma_f32_32x32x16_bf16 v[2:17], v[156:159], v[180:183], v[2:17]
	v_mfma_f32_32x32x16_bf16 v[2:17], v[156:159], v[184:187], v[2:17]
	global_load_dwordx4 v[156:159], v[20:21], off offset:1952
	s_waitcnt vmcnt(31)
; #define LAS __attribute__((address_space(3)))
; __device__ __forceinline__ void phase_norm2_route(const Frame& F, const Params& P, int l, int nrows, long long dctx) {
;     ...
; #pragma unroll
;         for (int q = 0; q < 8; ++q) { ahA[q] = *(const bf16x8*)(ph + q * 16); alA[q] = *(const bf16x8*)(pl + q * 16); }
; #pragma unroll
;         for (int bt = 0; bt < 8; bt += 2) {
; #pragma unroll
;             for (int q = 0; q < 8; ++q) { ahB[q] = *(const bf16x8*)(ph + ((bt + 1) * 8 + q) * 16); alB[q] = *(const bf16x8*)(pl + ((bt + 1) * 8 + q) * 16); }
; #pragma unroll
;             for (int q = 0; q < 8; ++q) { const int ks = bt * 8 + q;
;                 const bf16x8 wh = *(const LAS bf16x8*)(bh + ks * 16), wl = *(const LAS bf16x8*)(bl + ks * 16);
;                 acc = __builtin_amdgcn_mfma_f32_32x32x16_bf16(ahA[q], wh, acc, 0, 0, 0); acc = __builtin_amdgcn_mfma_f32_32x32x16_bf16(ahA[q], wl, acc, 0, 0, 0); acc = __builtin_amdgcn_mfma_f32_32x32x16_bf16(alA[q], wh, acc, 0, 0, 0); }
;             if (bt + 2 < 8) {
; #pragma unroll
;                 for (int q = 0; q < 8; ++q) { ahA[q] = *(const bf16x8*)(ph + ((bt + 2) * 8 + q) * 16); alA[q] = *(const bf16x8*)(pl + ((bt + 2) * 8 + q) * 16); }
;             }
; #pragma unroll
;             for (int q = 0; q < 8; ++q) { const int ks = (bt + 1) * 8 + q;
;                 const bf16x8 wh = *(const LAS bf16x8*)(bh + ks * 16), wl = *(const LAS bf16x8*)(bl + ks * 16);
;                 acc = __builtin_amdgcn_mfma_f32_32x32x16_bf16(ahB[q], wh, acc, 0, 0, 0); acc = __builtin_amdgcn_mfma_f32_32x32x16_bf16(ahB[q], wl, acc, 0, 0, 0); acc = __builtin_amdgcn_mfma_f32_32x32x16_bf16(alB[q], wh, acc, 0, 0, 0); }
;         }
	v_mfma_f32_32x32x16_bf16 v[2:17], v[160:163], v[180:183], v[2:17]
	global_load_dwordx4 v[160:163], v[18:19], off offset:1952
	ds_read_b128 v[180:183], v29 offset:1504
	ds_read_b128 v[184:187], v31 offset:1504
	s_waitcnt vmcnt(31) lgkmcnt(2)
	v_mfma_f32_32x32x16_bf16 v[2:17], v[164:167], v[38:41], v[2:17]
	v_mfma_f32_32x32x16_bf16 v[2:17], v[164:167], v[42:45], v[2:17]
	global_load_dwordx4 v[164:167], v[20:21], off offset:1984
	s_waitcnt vmcnt(31)
	v_mfma_f32_32x32x16_bf16 v[2:17], v[168:171], v[38:41], v[2:17]
	global_load_dwordx4 v[168:171], v[18:19], off offset:1984
	ds_read_b128 v[38:41], v29 offset:1536
	ds_read_b128 v[42:45], v31 offset:1536
	s_waitcnt vmcnt(31) lgkmcnt(2)
	v_mfma_f32_32x32x16_bf16 v[2:17], v[172:175], v[180:183], v[2:17]
	v_mfma_f32_32x32x16_bf16 v[2:17], v[172:175], v[184:187], v[2:17]
	global_load_dwordx4 v[172:175], v[20:21], off offset:2016
	s_waitcnt vmcnt(31)
	v_mfma_f32_32x32x16_bf16 v[2:17], v[176:179], v[180:183], v[2:17]
	global_load_dwordx4 v[176:179], v[18:19], off offset:2016
	ds_read_b128 v[180:183], v29 offset:1568
	ds_read_b128 v[184:187], v31 offset:1568
	s_waitcnt vmcnt(31) lgkmcnt(2)
	v_mfma_f32_32x32x16_bf16 v[2:17], v[48:51], v[38:41], v[2:17]
	v_mfma_f32_32x32x16_bf16 v[2:17], v[48:51], v[42:45], v[2:17]
	s_waitcnt vmcnt(30)
	v_mfma_f32_32x32x16_bf16 v[2:17], v[52:55], v[38:41], v[2:17]
	ds_read_b128 v[38:41], v29 offset:1600
	ds_read_b128 v[42:45], v31 offset:1600
	s_waitcnt vmcnt(29) lgkmcnt(2)
	v_mfma_f32_32x32x16_bf16 v[2:17], v[56:59], v[180:183], v[2:17]
	v_mfma_f32_32x32x16_bf16 v[2:17], v[56:59], v[184:187], v[2:17]
	s_waitcnt vmcnt(28)
	v_mfma_f32_32x32x16_bf16 v[2:17], v[60:63], v[180:183], v[2:17]
	ds_read_b128 v[180:183], v29 offset:1632
	ds_read_b128 v[184:187], v31 offset:1632
	s_waitcnt vmcnt(27) lgkmcnt(2)
	v_mfma_f32_32x32x16_bf16 v[2:17], v[64:67], v[38:41], v[2:17]
	v_mfma_f32_32x32x16_bf16 v[2:17], v[64:67], v[42:45], v[2:17]
	s_waitcnt vmcnt(26)
	v_mfma_f32_32x32x16_bf16 v[2:17], v[68:71], v[38:41], v[2:17]
	ds_read_b128 v[38:41], v29 offset:1664
	ds_read_b128 v[42:45], v31 offset:1664
	s_waitcnt vmcnt(25) lgkmcnt(2)
	v_mfma_f32_32x32x16_bf16 v[2:17], v[72:75], v[180:183], v[2:17]
	v_mfma_f32_32x32x16_bf16 v[2:17], v[72:75], v[184:187], v[2:17]
	s_waitcnt vmcnt(24)
	v_mfma_f32_32x32x16_bf16 v[2:17], v[76:79], v[180:183], v[2:17]
	ds_read_b128 v[180:183], v29 offset:1696
	ds_read_b128 v[184:187], v31 offset:1696
	s_waitcnt vmcnt(23) lgkmcnt(2)
	v_mfma_f32_32x32x16_bf16 v[2:17], v[80:83], v[38:41], v[2:17]
	v_mfma_f32_32x32x16_bf16 v[2:17], v[80:83], v[42:45], v[2:17]
	s_waitcnt vmcnt(22)
	v_mfma_f32_32x32x16_bf16 v[2:17], v[84:87], v[38:41], v[2:17]
	ds_read_b128 v[38:41], v29 offset:1728
	ds_read_b128 v[42:45], v31 offset:1728
	s_waitcnt vmcnt(21) lgkmcnt(2)
	v_mfma_f32_32x32x16_bf16 v[2:17], v[88:91], v[180:183], v[2:17]
	v_mfma_f32_32x32x16_bf16 v[2:17], v[88:91], v[184:187], v[2:17]
	s_waitcnt vmcnt(20)
	v_mfma_f32_32x32x16_bf16 v[2:17], v[92:95], v[180:183], v[2:17]
	ds_read_b128 v[180:183], v29 offset:1760
	ds_read_b128 v[184:187], v31 offset:1760
	s_waitcnt vmcnt(19) lgkmcnt(2)
	v_mfma_f32_32x32x16_bf16 v[2:17], v[96:99], v[38:41], v[2:17]
	v_mfma_f32_32x32x16_bf16 v[2:17], v[96:99], v[42:45], v[2:17]
	s_waitcnt vmcnt(18)
	v_mfma_f32_32x32x16_bf16 v[2:17], v[100:103], v[38:41], v[2:17]
	ds_read_b128 v[38:41], v29 offset:1792
	ds_read_b128 v[42:45], v31 offset:1792
	s_waitcnt vmcnt(17) lgkmcnt(2)
	v_mfma_f32_32x32x16_bf16 v[2:17], v[104:107], v[180:183], v[2:17]
	v_mfma_f32_32x32x16_bf16 v[2:17], v[104:107], v[184:187], v[2:17]
	s_waitcnt vmcnt(16)
	v_mfma_f32_32x32x16_bf16 v[2:17], v[108:111], v[180:183], v[2:17]
	ds_read_b128 v[180:183], v29 offset:1824
	ds_read_b128 v[184:187], v31 offset:1824
	s_waitcnt vmcnt(15) lgkmcnt(2)
	v_mfma_f32_32x32x16_bf16 v[2:17], v[112:115], v[38:41], v[2:17]
	v_mfma_f32_32x32x16_bf16 v[2:17], v[112:115], v[42:45], v[2:17]
	s_waitcnt vmcnt(14)
	v_mfma_f32_32x32x16_bf16 v[2:17], v[116:119], v[38:41], v[2:17]
	ds_read_b128 v[38:41], v29 offset:1856
	ds_read_b128 v[42:45], v31 offset:1856
	s_waitcnt vmcnt(13) lgkmcnt(2)
	v_mfma_f32_32x32x16_bf16 v[2:17], v[120:123], v[180:183], v[2:17]
	v_mfma_f32_32x32x16_bf16 v[2:17], v[120:123], v[184:187], v[2:17]
	s_waitcnt vmcnt(12)
	v_mfma_f32_32x32x16_bf16 v[2:17], v[124:127], v[180:183], v[2:17]
	ds_read_b128 v[180:183], v29 offset:1888
	ds_read_b128 v[184:187], v31 offset:1888
	s_waitcnt vmcnt(11) lgkmcnt(2)
	v_mfma_f32_32x32x16_bf16 v[2:17], v[128:131], v[38:41], v[2:17]
	v_mfma_f32_32x32x16_bf16 v[2:17], v[128:131], v[42:45], v[2:17]
	s_waitcnt vmcnt(10)
	v_mfma_f32_32x32x16_bf16 v[2:17], v[132:135], v[38:41], v[2:17]
	ds_read_b128 v[38:41], v29 offset:1920
	ds_read_b128 v[42:45], v31 offset:1920
	s_waitcnt vmcnt(9) lgkmcnt(2)
	v_mfma_f32_32x32x16_bf16 v[2:17], v[136:139], v[180:183], v[2:17]
	v_mfma_f32_32x32x16_bf16 v[2:17], v[136:139], v[184:187], v[2:17]
	s_waitcnt vmcnt(8)
	v_mfma_f32_32x32x16_bf16 v[2:17], v[140:143], v[180:183], v[2:17]
	ds_read_b128 v[180:183], v29 offset:1952
	ds_read_b128 v[184:187], v31 offset:1952
	s_waitcnt vmcnt(7) lgkmcnt(2)
	v_mfma_f32_32x32x16_bf16 v[2:17], v[148:151], v[38:41], v[2:17]
	v_mfma_f32_32x32x16_bf16 v[2:17], v[148:151], v[42:45], v[2:17]
	s_waitcnt vmcnt(6)
	v_mfma_f32_32x32x16_bf16 v[2:17], v[152:155], v[38:41], v[2:17]
	ds_read_b128 v[38:41], v29 offset:1984
	ds_read_b128 v[42:45], v31 offset:1984
	s_waitcnt vmcnt(5) lgkmcnt(2)
	v_mfma_f32_32x32x16_bf16 v[2:17], v[156:159], v[180:183], v[2:17]
	v_mfma_f32_32x32x16_bf16 v[2:17], v[156:159], v[184:187], v[2:17]
	s_waitcnt vmcnt(4)
; #define LAS __attribute__((address_space(3)))
; __device__ __forceinline__ void phase_norm2_route(const Frame& F, const Params& P, int l, int nrows, long long dctx) {
;     ...
;             for (int q = 0; q < 8; ++q) { const int ks = bt * 8 + q;
;                 const bf16x8 wh = *(const LAS bf16x8*)(bh + ks * 16), wl = *(const LAS bf16x8*)(bl + ks * 16);
;                 acc = __builtin_amdgcn_mfma_f32_32x32x16_bf16(ahA[q], wh, acc, 0, 0, 0); acc = __builtin_amdgcn_mfma_f32_32x32x16_bf16(ahA[q], wl, acc, 0, 0, 0); acc = __builtin_amdgcn_mfma_f32_32x32x16_bf16(alA[q], wh, acc, 0, 0, 0); }
;             if (bt + 2 < 8) {
; #pragma unroll
;                 for (int q = 0; q < 8; ++q) { ahA[q] = *(const bf16x8*)(ph + ((bt + 2) * 8 + q) * 16); alA[q] = *(const bf16x8*)(pl + ((bt + 2) * 8 + q) * 16); }
;             }
; #pragma unroll
;             for (int q = 0; q < 8; ++q) { const int ks = (bt + 1) * 8 + q;
;                 const bf16x8 wh = *(const LAS bf16x8*)(bh + ks * 16), wl = *(const LAS bf16x8*)(bl + ks * 16);
;                 acc = __builtin_amdgcn_mfma_f32_32x32x16_bf16(ahB[q], wh, acc, 0, 0, 0); acc = __builtin_amdgcn_mfma_f32_32x32x16_bf16(ahB[q], wl, acc, 0, 0, 0); acc = __builtin_amdgcn_mfma_f32_32x32x16_bf16(alB[q], wh, acc, 0, 0, 0); }
;         }
;     ...
;         for (int r = 0; r < 16; ++r) {
;             float v = acc[r] + bias;
;             float tv[4]; int ti[4];
; #pragma unroll
;             for (int k = 0; k < 4; ++k) {
;                 float bv = v; int bi = r32;
;     ...
;                 RT_STEP(DPP_X1); RT_STEP(DPP_X2); RT_STEP(DPP_HMIR); RT_STEP(DPP_MIR);
;     ...
;                 {
;                     const auto rv = __builtin_amdgcn_permlane16_swap(__float_as_uint(bv), __float_as_uint(bv), false, false);
;                     const auto ri = __builtin_amdgcn_permlane16_swap((unsigned)bi, (unsigned)bi, false, false);
;                     const float v0 = __uint_as_float(rv[0]), v1 = __uint_as_float(rv[1]); const int i0 = (int)ri[0], i1 = (int)ri[1];
;                     const bool take1 = (v1 > v0) || (v1 == v0 && i1 < i0);
;                     bv = take1 ? v1 : v0; bi = take1 ? i1 : i0;
;                 }
;                 tv[k] = bv; ti[k] = bi;
;                 v = (r32 == bi) ? -3.0e38f : v;
	v_mfma_f32_32x32x16_bf16 v[2:17], v[160:163], v[180:183], v[2:17]
	ds_read_b128 v[180:183], v29 offset:2016
	ds_read_b128 v[184:187], v31 offset:2016
	s_waitcnt vmcnt(3) lgkmcnt(2)
	v_mfma_f32_32x32x16_bf16 v[2:17], v[164:167], v[38:41], v[2:17]
	v_mfma_f32_32x32x16_bf16 v[2:17], v[164:167], v[42:45], v[2:17]
	s_waitcnt vmcnt(2)
	v_mfma_f32_32x32x16_bf16 v[2:17], v[168:171], v[38:41], v[2:17]
	s_waitcnt vmcnt(1) lgkmcnt(0)
	v_mfma_f32_32x32x16_bf16 v[2:17], v[172:175], v[180:183], v[2:17]
	v_mfma_f32_32x32x16_bf16 v[2:17], v[172:175], v[184:187], v[2:17]
	s_waitcnt vmcnt(0)
	v_mfma_f32_32x32x16_bf16 v[2:17], v[176:179], v[180:183], v[2:17]
	v_mov_b32_dpp v18, v1 quad_perm:[1,0,3,2] row_mask:0xf bank_mask:0xf bound_ctrl:1
	s_nop 10
	v_add_f32_e32 v19, v28, v2
	s_nop 1
	v_mov_b32_dpp v2, v19 quad_perm:[1,0,3,2] row_mask:0xf bank_mask:0xf bound_ctrl:1
	v_cmp_nlt_f32_e32 vcc, v19, v2
	s_and_saveexec_b64 s[18:19], vcc
	v_cmp_eq_f32_e32 vcc, v19, v2
	v_cmp_lt_i32_e64 s[74:75], v18, v1
	s_and_b64 s[0:1], vcc, s[74:75]
	s_orn2_b64 s[22:23], s[0:1], exec
	s_or_b64 exec, exec, s[18:19]
	v_cndmask_b32_e64 v2, v19, v2, s[22:23]
	v_cndmask_b32_e64 v18, v1, v18, s[22:23]
	s_nop 0
	v_mov_b32_dpp v20, v2 quad_perm:[2,3,0,1] row_mask:0xf bank_mask:0xf bound_ctrl:1
	v_mov_b32_dpp v21, v18 quad_perm:[2,3,0,1] row_mask:0xf bank_mask:0xf bound_ctrl:1
	v_cmp_nlt_f32_e32 vcc, v2, v20
	s_and_saveexec_b64 s[18:19], vcc
	v_cmp_eq_f32_e32 vcc, v2, v20
	v_cmp_lt_i32_e64 s[74:75], v21, v18
	s_and_b64 s[0:1], vcc, s[74:75]
	s_orn2_b64 s[8:9], s[0:1], exec
	s_or_b64 exec, exec, s[18:19]
	v_cndmask_b32_e64 v2, v2, v20, s[8:9]
	v_cndmask_b32_e64 v18, v18, v21, s[8:9]
	s_mov_b64 s[8:9], -1
	v_mov_b32_dpp v20, v2 row_half_mirror row_mask:0xf bank_mask:0xf bound_ctrl:1
	v_mov_b32_dpp v21, v18 row_half_mirror row_mask:0xf bank_mask:0xf bound_ctrl:1
	v_cmp_nlt_f32_e32 vcc, v2, v20
	s_mov_b64 s[22:23], -1
	s_and_saveexec_b64 s[18:19], vcc
	v_cmp_eq_f32_e32 vcc, v2, v20
	v_cmp_lt_i32_e64 s[74:75], v21, v18
	s_and_b64 s[0:1], vcc, s[74:75]
	s_orn2_b64 s[22:23], s[0:1], exec
	s_or_b64 exec, exec, s[18:19]
	v_cndmask_b32_e64 v2, v2, v20, s[22:23]
	v_cndmask_b32_e64 v18, v18, v21, s[22:23]
	s_nop 0
	v_mov_b32_dpp v20, v2 row_mirror row_mask:0xf bank_mask:0xf bound_ctrl:1
	v_mov_b32_dpp v21, v18 row_mirror row_mask:0xf bank_mask:0xf bound_ctrl:1
	v_cmp_nlt_f32_e32 vcc, v2, v20
	s_and_saveexec_b64 s[18:19], vcc
	v_cmp_eq_f32_e32 vcc, v2, v20
	v_cmp_lt_i32_e64 s[74:75], v21, v18
	s_and_b64 s[0:1], vcc, s[74:75]
	s_orn2_b64 s[8:9], s[0:1], exec
	s_or_b64 exec, exec, s[18:19]
	v_cndmask_b32_e64 v2, v2, v20, s[8:9]
	v_cndmask_b32_e64 v18, v18, v21, s[8:9]
	v_mov_b32_e32 v21, v2
	s_nop 1
	v_permlane16_swap_b32_e32 v2, v21
	v_mov_b32_e32 v20, v18
	s_nop 1
	v_permlane16_swap_b32_e32 v18, v20
	v_cmp_ngt_f32_e32 vcc, v21, v2
	s_mov_b64 s[18:19], -1
	s_mov_b64 s[8:9], -1
	s_and_saveexec_b64 s[22:23], vcc
	v_cmp_eq_f32_e32 vcc, v21, v2
	v_cmp_lt_i32_e64 s[74:75], v20, v18
	s_and_b64 s[0:1], vcc, s[74:75]
	s_orn2_b64 s[8:9], s[0:1], exec
	s_or_b64 exec, exec, s[22:23]
	v_cndmask_b32_e64 v18, v18, v20, s[8:9]
	v_cmp_ne_u32_e32 vcc, v1, v18
	v_mov_b32_dpp v26, v1 quad_perm:[1,0,3,2] row_mask:0xf bank_mask:0xf bound_ctrl:1
	s_nop 0
	v_cndmask_b32_e32 v20, v251, v19, vcc
	s_nop 1
	v_mov_b32_dpp v19, v20 quad_perm:[1,0,3,2] row_mask:0xf bank_mask:0xf bound_ctrl:1
	v_cmp_nlt_f32_e32 vcc, v20, v19
	s_and_saveexec_b64 s[22:23], vcc
	v_cmp_eq_f32_e32 vcc, v20, v19
	v_cmp_lt_i32_e64 s[74:75], v26, v1
	s_and_b64 s[0:1], s[74:75], vcc
	s_orn2_b64 s[18:19], s[0:1], exec
	s_or_b64 exec, exec, s[22:23]
	v_cndmask_b32_e64 v19, v20, v19, s[18:19]
	v_cndmask_b32_e64 v26, v1, v26, s[18:19]
	s_mov_b64 s[18:19], -1
	v_mov_b32_dpp v27, v19 quad_perm:[2,3,0,1] row_mask:0xf bank_mask:0xf bound_ctrl:1
	v_mov_b32_dpp v33, v26 quad_perm:[2,3,0,1] row_mask:0xf bank_mask:0xf bound_ctrl:1
	v_cmp_nlt_f32_e32 vcc, v19, v27
	s_mov_b64 s[24:25], -1
	s_and_saveexec_b64 s[22:23], vcc
	v_cmp_eq_f32_e32 vcc, v19, v27
	v_cmp_lt_i32_e64 s[74:75], v33, v26
	s_and_b64 s[0:1], vcc, s[74:75]
	s_orn2_b64 s[24:25], s[0:1], exec
	s_or_b64 exec, exec, s[22:23]
	v_cndmask_b32_e64 v19, v19, v27, s[24:25]
	v_cndmask_b32_e64 v27, v26, v33, s[24:25]
	s_nop 0
	v_mov_b32_dpp v26, v19 row_half_mirror row_mask:0xf bank_mask:0xf bound_ctrl:1
	v_mov_b32_dpp v33, v27 row_half_mirror row_mask:0xf bank_mask:0xf bound_ctrl:1
	v_cmp_nlt_f32_e32 vcc, v19, v26
	s_and_saveexec_b64 s[22:23], vcc
	v_cmp_eq_f32_e32 vcc, v19, v26
	v_cmp_lt_i32_e64 s[74:75], v33, v27
	s_and_b64 s[0:1], vcc, s[74:75]
	s_orn2_b64 s[18:19], s[0:1], exec
	s_or_b64 exec, exec, s[22:23]
	v_cndmask_b32_e64 v26, v19, v26, s[18:19]
	v_cndmask_b32_e64 v19, v27, v33, s[18:19]
	s_mov_b64 s[18:19], -1
	v_mov_b32_dpp v27, v26 row_mirror row_mask:0xf bank_mask:0xf bound_ctrl:1
	v_mov_b32_dpp v33, v19 row_mirror row_mask:0xf bank_mask:0xf bound_ctrl:1
	v_cmp_nlt_f32_e32 vcc, v26, v27
	s_mov_b64 s[24:25], -1
	s_and_saveexec_b64 s[22:23], vcc
	v_cmp_eq_f32_e32 vcc, v26, v27
	v_cmp_lt_i32_e64 s[74:75], v33, v19
	s_and_b64 s[0:1], vcc, s[74:75]
	s_orn2_b64 s[24:25], s[0:1], exec
	s_or_b64 exec, exec, s[22:23]
	v_cndmask_b32_e64 v27, v26, v27, s[24:25]
	v_cndmask_b32_e64 v19, v19, v33, s[24:25]
	v_mov_b32_e32 v33, v27
	s_nop 1
	v_permlane16_swap_b32_e32 v27, v33
	v_mov_b32_e32 v26, v19
	s_nop 1
	v_permlane16_swap_b32_e32 v19, v26
	v_cmp_ngt_f32_e32 vcc, v33, v27
	s_and_saveexec_b64 s[22:23], vcc
	v_cmp_eq_f32_e32 vcc, v33, v27
	v_cmp_lt_i32_e64 s[74:75], v26, v19
	s_and_b64 s[0:1], vcc, s[74:75]
	s_orn2_b64 s[18:19], s[0:1], exec
	s_or_b64 exec, exec, s[22:23]
	v_cndmask_b32_e64 v19, v19, v26, s[18:19]
;     __device__ __forceinline__ int* sele() const { return (int*)(ws + WS_SELE); }
;     __device__ __forceinline__ float* selw() const { return (float*)(ws + WS_SELW); }
; __device__ __forceinline__ int crow(int r, int hi) { return (r & 3) + 8 * (r >> 2) + 4 * hi; }
; #define RT_STEP(CTRL) do { const float ov = dpp_f<CTRL>(bv); const int oi = dpp_i<CTRL>(bi); const bool take = (ov > bv) || (ov == bv && oi < bi); bv = take ? ov : bv; bi = take ? oi : bi; } while (0)
; __device__ __forceinline__ void phase_norm2_route(const Frame& F, const Params& P, int l, int nrows, long long dctx) {
;     ...
;             float v = acc[r] + bias;
;             float tv[4]; int ti[4];
; #pragma unroll
;             for (int k = 0; k < 4; ++k) {
;                 float bv = v; int bi = r32;
;     ...
;                 RT_STEP(DPP_X1); RT_STEP(DPP_X2); RT_STEP(DPP_HMIR); RT_STEP(DPP_MIR);
;     ...
;                 {
;                     const auto rv = __builtin_amdgcn_permlane16_swap(__float_as_uint(bv), __float_as_uint(bv), false, false);
;                     const auto ri = __builtin_amdgcn_permlane16_swap((unsigned)bi, (unsigned)bi, false, false);
;                     const float v0 = __uint_as_float(rv[0]), v1 = __uint_as_float(rv[1]); const int i0 = (int)ri[0], i1 = (int)ri[1];
;                     const bool take1 = (v1 > v0) || (v1 == v0 && i1 < i0);
;                     bv = take1 ? v1 : v0; bi = take1 ? i1 : i0;
;                 }
;                 tv[k] = bv; ti[k] = bi;
;                 v = (r32 == bi) ? -3.0e38f : v;
;             }
;             const int row = rowbase + at::crow(r, hi);
;             if (r32 == r && row < r1) {
;                 float w4[4], den = 0.f;
; #pragma unroll
;                 for (int k = 0; k < 4; ++k) { w4[k] = __expf(tv[k] - tv[0]); den += w4[k]; }
;                 const float inv = 1.f / den;
; #pragma unroll
;                 for (int k = 0; k < 4; ++k) {
;                     F.sele()[(size_t)row * 4 + k] = ti[k]; F.selw()[(size_t)row * 4 + k] = w4[k] * inv;
;                     __hip_atomic_fetch_add(&hist[ti[k]], 1, __ATOMIC_RELAXED, __HIP_MEMORY_SCOPE_WORKGROUP);
;                 }
	v_cmp_ne_u32_e32 vcc, v1, v19
	v_mov_b32_dpp v34, v1 quad_perm:[1,0,3,2] row_mask:0xf bank_mask:0xf bound_ctrl:1
	s_mov_b64 s[22:23], -1
	v_cndmask_b32_e32 v26, v251, v20, vcc
	s_mov_b64 s[28:29], -1
	s_nop 0
	v_mov_b32_dpp v20, v26 quad_perm:[1,0,3,2] row_mask:0xf bank_mask:0xf bound_ctrl:1
	v_cmp_nlt_f32_e32 vcc, v26, v20
	s_and_saveexec_b64 s[24:25], vcc
	v_cmp_eq_f32_e32 vcc, v26, v20
	v_cmp_lt_i32_e64 s[74:75], v34, v1
	s_and_b64 s[0:1], s[74:75], vcc
	s_orn2_b64 s[28:29], s[0:1], exec
	s_or_b64 exec, exec, s[24:25]
	v_cndmask_b32_e64 v20, v26, v20, s[28:29]
	v_cndmask_b32_e64 v34, v1, v34, s[28:29]
	s_nop 0
	v_mov_b32_dpp v35, v20 quad_perm:[2,3,0,1] row_mask:0xf bank_mask:0xf bound_ctrl:1
	v_mov_b32_dpp v36, v34 quad_perm:[2,3,0,1] row_mask:0xf bank_mask:0xf bound_ctrl:1
	v_cmp_nlt_f32_e32 vcc, v20, v35
	s_and_saveexec_b64 s[24:25], vcc
	v_cmp_eq_f32_e32 vcc, v20, v35
	v_cmp_lt_i32_e64 s[74:75], v36, v34
	s_and_b64 s[0:1], vcc, s[74:75]
	s_orn2_b64 s[22:23], s[0:1], exec
	s_or_b64 exec, exec, s[24:25]
	v_cndmask_b32_e64 v20, v20, v35, s[22:23]
	v_cndmask_b32_e64 v34, v34, v36, s[22:23]
	s_mov_b64 s[22:23], -1
	v_mov_b32_dpp v35, v20 row_half_mirror row_mask:0xf bank_mask:0xf bound_ctrl:1
	v_mov_b32_dpp v36, v34 row_half_mirror row_mask:0xf bank_mask:0xf bound_ctrl:1
	v_cmp_nlt_f32_e32 vcc, v20, v35
	s_mov_b64 s[28:29], -1
	s_and_saveexec_b64 s[24:25], vcc
	v_cmp_eq_f32_e32 vcc, v20, v35
	v_cmp_lt_i32_e64 s[74:75], v36, v34
	s_and_b64 s[0:1], vcc, s[74:75]
	s_orn2_b64 s[28:29], s[0:1], exec
	s_or_b64 exec, exec, s[24:25]
	v_cndmask_b32_e64 v35, v20, v35, s[28:29]
	v_cndmask_b32_e64 v20, v34, v36, s[28:29]
	s_nop 0
	v_mov_b32_dpp v34, v35 row_mirror row_mask:0xf bank_mask:0xf bound_ctrl:1
	v_mov_b32_dpp v36, v20 row_mirror row_mask:0xf bank_mask:0xf bound_ctrl:1
	v_cmp_nlt_f32_e32 vcc, v35, v34
	s_and_saveexec_b64 s[24:25], vcc
	v_cmp_eq_f32_e32 vcc, v35, v34
	v_cmp_lt_i32_e64 s[74:75], v36, v20
	s_and_b64 s[0:1], vcc, s[74:75]
	s_orn2_b64 s[22:23], s[0:1], exec
	s_or_b64 exec, exec, s[24:25]
	v_cndmask_b32_e64 v34, v35, v34, s[22:23]
	v_cndmask_b32_e64 v20, v20, v36, s[22:23]
	v_mov_b32_e32 v35, v34
	s_nop 1
	v_permlane16_swap_b32_e32 v34, v35
	v_mov_b32_e32 v36, v20
	s_nop 1
	v_permlane16_swap_b32_e32 v20, v36
	v_cmp_ngt_f32_e32 vcc, v35, v34
	s_mov_b64 s[24:25], -1
	s_mov_b64 s[22:23], -1
	s_and_saveexec_b64 s[28:29], vcc
	v_cmp_eq_f32_e32 vcc, v35, v34
	v_cmp_lt_i32_e64 s[74:75], v36, v20
	s_and_b64 s[0:1], vcc, s[74:75]
	s_orn2_b64 s[22:23], s[0:1], exec
	s_or_b64 exec, exec, s[28:29]
	v_cndmask_b32_e64 v20, v20, v36, s[22:23]
	v_cmp_ne_u32_e32 vcc, v1, v20
	v_mov_b32_dpp v37, v1 quad_perm:[1,0,3,2] row_mask:0xf bank_mask:0xf bound_ctrl:1
	s_nop 0
	v_cndmask_b32_e32 v26, v251, v26, vcc
	s_nop 1
	v_mov_b32_dpp v36, v26 quad_perm:[1,0,3,2] row_mask:0xf bank_mask:0xf bound_ctrl:1
	v_cmp_nlt_f32_e32 vcc, v26, v36
	s_and_saveexec_b64 s[28:29], vcc
	v_cmp_eq_f32_e32 vcc, v26, v36
	v_cmp_lt_i32_e64 s[74:75], v37, v1
	s_and_b64 s[0:1], s[74:75], vcc
	s_orn2_b64 s[24:25], s[0:1], exec
	s_or_b64 exec, exec, s[28:29]
	v_cndmask_b32_e64 v26, v26, v36, s[24:25]
	v_cndmask_b32_e64 v36, v1, v37, s[24:25]
	s_mov_b64 s[24:25], -1
	v_mov_b32_dpp v37, v26 quad_perm:[2,3,0,1] row_mask:0xf bank_mask:0xf bound_ctrl:1
	v_mov_b32_dpp v38, v36 quad_perm:[2,3,0,1] row_mask:0xf bank_mask:0xf bound_ctrl:1
	v_cmp_nlt_f32_e32 vcc, v26, v37
	s_mov_b64 s[30:31], -1
	s_and_saveexec_b64 s[28:29], vcc
	v_cmp_eq_f32_e32 vcc, v26, v37
	v_cmp_lt_i32_e64 s[74:75], v38, v36
	s_and_b64 s[0:1], vcc, s[74:75]
	s_orn2_b64 s[30:31], s[0:1], exec
	s_or_b64 exec, exec, s[28:29]
	v_cndmask_b32_e64 v26, v26, v37, s[30:31]
	v_cndmask_b32_e64 v36, v36, v38, s[30:31]
	s_nop 0
	v_mov_b32_dpp v37, v26 row_half_mirror row_mask:0xf bank_mask:0xf bound_ctrl:1
	v_mov_b32_dpp v38, v36 row_half_mirror row_mask:0xf bank_mask:0xf bound_ctrl:1
	v_cmp_nlt_f32_e32 vcc, v26, v37
	s_and_saveexec_b64 s[28:29], vcc
	v_cmp_eq_f32_e32 vcc, v26, v37
	v_cmp_lt_i32_e64 s[74:75], v38, v36
	s_and_b64 s[0:1], vcc, s[74:75]
	s_orn2_b64 s[24:25], s[0:1], exec
	s_or_b64 exec, exec, s[28:29]
	v_cndmask_b32_e64 v26, v26, v37, s[24:25]
	v_cndmask_b32_e64 v36, v36, v38, s[24:25]
	s_mov_b64 s[28:29], -1
	v_mov_b32_dpp v37, v26 row_mirror row_mask:0xf bank_mask:0xf bound_ctrl:1
	v_mov_b32_dpp v38, v36 row_mirror row_mask:0xf bank_mask:0xf bound_ctrl:1
	v_cmp_nlt_f32_e32 vcc, v26, v37
	s_mov_b64 s[30:31], -1
	s_and_saveexec_b64 s[24:25], vcc
	v_cmp_eq_f32_e32 vcc, v26, v37
	v_cmp_lt_i32_e64 s[74:75], v38, v36
	s_and_b64 s[0:1], vcc, s[74:75]
	s_orn2_b64 s[30:31], s[0:1], exec
	s_or_b64 exec, exec, s[24:25]
	v_cndmask_b32_e64 v36, v36, v38, s[30:31]
	v_cndmask_b32_e64 v38, v26, v37, s[30:31]
	v_mov_b32_e32 v39, v38
	s_nop 1
	v_permlane16_swap_b32_e32 v38, v39
	v_mov_b32_e32 v37, v36
	s_nop 1
	v_permlane16_swap_b32_e32 v36, v37
	v_cmp_ngt_f32_e32 vcc, v39, v38
	s_and_saveexec_b64 s[24:25], vcc
	v_cmp_eq_f32_e32 vcc, v39, v38
	v_cmp_lt_i32_e64 s[74:75], v37, v36
	s_and_b64 s[0:1], vcc, s[74:75]
	s_orn2_b64 s[28:29], s[0:1], exec
	s_or_b64 exec, exec, s[24:25]
	v_add_u32_e32 v26, s89, v32
	v_cmp_gt_i32_e32 vcc, s85, v26
	s_and_b64 s[0:1], s[42:43], vcc
	s_and_saveexec_b64 s[24:25], s[0:1]
	s_cbranch_execz .LBB0_978
	v_cndmask_b32_e64 v27, v27, v33, s[18:19]
	v_cndmask_b32_e64 v2, v2, v21, s[8:9]
	v_sub_f32_e32 v33, v2, v2
	v_sub_f32_e32 v27, v27, v2
	v_cndmask_b32_e64 v40, v34, v35, s[22:23]
	v_mul_f32_e32 v33, 0x3fb8aa3b, v33
	v_mul_f32_e32 v27, 0x3fb8aa3b, v27
	v_cndmask_b32_e64 v21, v38, v39, s[28:29]
	v_exp_f32_e32 v34, v33
	v_exp_f32_e32 v35, v27
	v_sub_f32_e32 v27, v40, v2
	v_mul_f32_e32 v27, 0x3fb8aa3b, v27
	v_sub_f32_e32 v2, v21, v2
	v_exp_f32_e32 v38, v27
	v_mul_f32_e32 v2, 0x3fb8aa3b, v2
	v_exp_f32_e32 v39, v2
	v_add_f32_e32 v2, 0, v34
	v_add_f32_e32 v2, v2, v35
	v_add_f32_e32 v2, v2, v38
	v_add_f32_e32 v2, v2, v39
	v_div_scale_f32 v27, s[0:1], v2, v2, 1.0
	v_rcp_f32_e32 v33, v27
	v_cndmask_b32_e64 v21, v36, v37, s[28:29]
	s_add_i32 s0, 0, 0x20400
	v_fma_f32 v36, -v27, v33, 1.0
	v_fmac_f32_e32 v33, v36, v33
	v_div_scale_f32 v36, vcc, 1.0, v2, 1.0
	v_mul_f32_e32 v37, v36, v33
	v_fma_f32 v40, -v27, v37, v36
	v_fmac_f32_e32 v37, v40, v33
	v_fma_f32 v27, -v27, v37, v36
	v_div_fmas_f32 v27, v27, v33, v37
	v_div_fixup_f32 v2, v27, v2, 1.0
	v_ashrrev_i32_e32 v27, 31, v26
	v_lshlrev_b64 v[36:37], 4, v[26:27]
	v_lshl_add_u32 v27, v18, 2, s0
	ds_add_u32 v27, v228
	v_lshl_add_u32 v27, v19, 2, s0
	v_lshl_add_u64 v[40:41], s[80:81], 0, v[36:37]
	v_lshl_add_u64 v[42:43], s[82:83], 0, v[36:37]
	v_pk_mul_f32 v[34:35], v[34:35], v[2:3] op_sel_hi:[1,0]
	ds_add_u32 v27, v228
	v_lshl_add_u32 v27, v20, 2, s0
	v_pk_mul_f32 v[36:37], v[38:39], v[2:3] op_sel_hi:[1,0]
	ds_add_u32 v27, v228
	global_store_dwordx4 v[40:41], v[18:21], off
	global_store_dwordx4 v[42:43], v[34:37], off
	v_lshl_add_u32 v2, v21, 2, s0
	ds_add_u32 v2, v228
